# in-proj GEMM epilogue: bias vectors requested at the unit's K-loop start (no load+wait in the epilogue), on top of v19
# speedup vs baseline: 1.0050x; 1.0042x over previous
.LBB0_343:
	s_ashr_i32 s51, s50, 31
	v_mov_b64_e32 v[2:3], 0x77a
	s_lshl_b64 s[14:15], s[50:51], 19
	v_cmp_lt_i64_e32 vcc, s[52:53], v[2:3]
	s_add_u32 s52, s42, s14
	s_addc_u32 s53, s43, s15
	s_and_b64 s[14:15], vcc, exec
	s_cselect_b32 s9, s53, s57
	s_cselect_b32 s14, s52, s56
	s_ashr_i32 s49, s48, 31
	s_lshl_b64 s[54:55], s[48:49], 19
	s_add_u32 s54, s63, s54
	s_addc_u32 s55, s64, s55
	s_and_b64 s[58:59], vcc, exec
	s_cselect_b32 s15, s55, s39
	s_cselect_b32 s35, s54, s38
	s_add_u32 s37, s38, 0x100
	s_addc_u32 s49, s39, 0
	s_add_u32 s38, s56, 0x40080
	v_mov_b32_e32 v2, 0
	s_addc_u32 s39, s57, 0
	s_mov_b32 s51, -2
	v_mov_b32_e32 v3, v2
	v_mov_b32_e32 v4, v2
	v_mov_b32_e32 v5, v2
	v_mov_b32_e32 v6, v2
	v_mov_b32_e32 v7, v2
	v_mov_b32_e32 v8, v2
	v_mov_b32_e32 v9, v2
	v_mov_b32_e32 v10, v2
	v_mov_b32_e32 v11, v2
	v_mov_b32_e32 v12, v2
	v_mov_b32_e32 v13, v2
	v_mov_b32_e32 v14, v2
	v_mov_b32_e32 v15, v2
	v_mov_b32_e32 v16, v2
	v_mov_b32_e32 v17, v2
	v_mov_b32_e32 v18, v2
	v_mov_b32_e32 v19, v2
	v_mov_b32_e32 v20, v2
	v_mov_b32_e32 v21, v2
	v_mov_b32_e32 v22, v2
	v_mov_b32_e32 v23, v2
	v_mov_b32_e32 v24, v2
	v_mov_b32_e32 v25, v2
	v_mov_b32_e32 v26, v2
	v_mov_b32_e32 v27, v2
	v_mov_b32_e32 v28, v2
	v_mov_b32_e32 v29, v2
	v_mov_b32_e32 v30, v2
	v_mov_b32_e32 v31, v2
	v_mov_b32_e32 v32, v2
	v_mov_b32_e32 v33, v2
	v_mov_b32_e32 v66, v2
	v_mov_b32_e32 v67, v2
	v_mov_b32_e32 v68, v2
	v_mov_b32_e32 v69, v2
	v_mov_b32_e32 v70, v2
	v_mov_b32_e32 v71, v2
	v_mov_b32_e32 v72, v2
	v_mov_b32_e32 v73, v2
	v_mov_b32_e32 v74, v2
	v_mov_b32_e32 v75, v2
	v_mov_b32_e32 v76, v2
	v_mov_b32_e32 v77, v2
	v_mov_b32_e32 v78, v2
	v_mov_b32_e32 v79, v2
	v_mov_b32_e32 v80, v2
	v_mov_b32_e32 v81, v2
	v_mov_b32_e32 v82, v2
	v_mov_b32_e32 v83, v2
	v_mov_b32_e32 v84, v2
	v_mov_b32_e32 v85, v2
	v_mov_b32_e32 v86, v2
	v_mov_b32_e32 v87, v2
	v_mov_b32_e32 v88, v2
	v_mov_b32_e32 v89, v2
	v_mov_b32_e32 v90, v2
	v_mov_b32_e32 v91, v2
	v_mov_b32_e32 v92, v2
	v_mov_b32_e32 v93, v2
	v_mov_b32_e32 v94, v2
	v_mov_b32_e32 v95, v2
	v_mov_b32_e32 v96, v2
	v_mov_b32_e32 v97, v2
	v_mov_b32_e32 v34, v2
	v_mov_b32_e32 v35, v2
	v_mov_b32_e32 v36, v2
	v_mov_b32_e32 v37, v2
	v_mov_b32_e32 v38, v2
	v_mov_b32_e32 v39, v2
	v_mov_b32_e32 v40, v2
	v_mov_b32_e32 v41, v2
	v_mov_b32_e32 v42, v2
	v_mov_b32_e32 v43, v2
	v_mov_b32_e32 v44, v2
	v_mov_b32_e32 v45, v2
	v_mov_b32_e32 v46, v2
	v_mov_b32_e32 v47, v2
	v_mov_b32_e32 v48, v2
	v_mov_b32_e32 v49, v2
	v_mov_b32_e32 v50, v2
	v_mov_b32_e32 v51, v2
	v_mov_b32_e32 v52, v2
	v_mov_b32_e32 v53, v2
	v_mov_b32_e32 v54, v2
	v_mov_b32_e32 v55, v2
	v_mov_b32_e32 v56, v2
	v_mov_b32_e32 v57, v2
	v_mov_b32_e32 v58, v2
	v_mov_b32_e32 v59, v2
	v_mov_b32_e32 v60, v2
	v_mov_b32_e32 v61, v2
	v_mov_b32_e32 v62, v2
	v_mov_b32_e32 v63, v2
	v_mov_b32_e32 v64, v2
	v_mov_b32_e32 v65, v2
	v_mov_b32_e32 v98, v2
	v_mov_b32_e32 v99, v2
	v_mov_b32_e32 v100, v2
	v_mov_b32_e32 v101, v2
	v_mov_b32_e32 v102, v2
	v_mov_b32_e32 v103, v2
	v_mov_b32_e32 v104, v2
	v_mov_b32_e32 v105, v2
	v_mov_b32_e32 v106, v2
	v_mov_b32_e32 v107, v2
	v_mov_b32_e32 v108, v2
	v_mov_b32_e32 v109, v2
	v_mov_b32_e32 v110, v2
	v_mov_b32_e32 v111, v2
	v_mov_b32_e32 v112, v2
	v_mov_b32_e32 v113, v2
	v_mov_b32_e32 v114, v2
	v_mov_b32_e32 v115, v2
	v_mov_b32_e32 v116, v2
	v_mov_b32_e32 v117, v2
	v_mov_b32_e32 v118, v2
	v_mov_b32_e32 v119, v2
	v_mov_b32_e32 v120, v2
	v_mov_b32_e32 v121, v2
	v_mov_b32_e32 v122, v2
	v_mov_b32_e32 v123, v2
	v_mov_b32_e32 v124, v2
	v_mov_b32_e32 v125, v2
	v_mov_b32_e32 v126, v2
	v_mov_b32_e32 v127, v2
	v_mov_b32_e32 v128, v2
	v_mov_b32_e32 v129, v2
	s_lshl_b32 s96, s34, 8
	s_or_b32 s96, s96, s82
	v_or_b32_e32 v252, s96, v155
	v_add_u32_e32 v253, 0x80, v252
	v_min_u32_e32 v252, 0x1cb8, v252
	v_min_u32_e32 v253, 0x1cb8, v253
	v_lshlrev_b32_e32 v252, 2, v252
	v_lshlrev_b32_e32 v253, 2, v253
	global_load_dwordx4 v[240:243], v252, s[30:31]
	global_load_dwordx4 v[244:247], v252, s[30:31] offset:16
	global_load_dwordx4 v[248:251], v253, s[30:31]
	global_load_dwordx4 v[222:225], v253, s[30:31] offset:16
.LBB0_344:
	s_add_u32 s56, s38, 0xfffc0080
	s_addc_u32 s57, s39, -1
	s_add_i32 s96, 0, 0x10040
	v_add_u32_e32 v158, s96, v156
	ds_read_b128 v[130:133], v158
	ds_read_b128 v[134:137], v158 offset:1024
	ds_read_b128 v[150:153], v158 offset:2048
	ds_read_b128 v[158:161], v158 offset:3072
	s_cmp_eq_u32 s51, 12
	s_cselect_b32 s59, s9, s57
	s_cselect_b32 s58, s14, s56
	s_cselect_b32 s57, s15, s49
	s_cselect_b32 s56, s35, s37
	v_lshl_add_u64 v[198:199], s[38:39], 0, v[148:149]
	s_add_i32 m0, s66, 0xc040
	ds_read_b128 v[162:165], v157 offset:64
	ds_read_b128 v[166:169], v157 offset:1088
	ds_read_b128 v[170:173], v157 offset:2112
	ds_read_b128 v[174:177], v157 offset:3136
	ds_read_b128 v[178:181], v157 offset:4160
	ds_read_b128 v[182:185], v157 offset:5184
	ds_read_b128 v[186:189], v157 offset:6208
	ds_read_b128 v[190:193], v157 offset:7232
	global_load_lds_dwordx4 v[198:199], off
	v_lshl_add_u64 v[198:199], s[38:39], 0, v[146:147]
	s_add_i32 m0, s66, 0xe040
	s_nop 0
	global_load_lds_dwordx4 v[198:199], off
	s_waitcnt lgkmcnt(8)
	s_barrier
	s_waitcnt lgkmcnt(0)
	s_setprio 1
	s_waitcnt lgkmcnt(0)
	v_mfma_f32_16x16x32_bf16 v[126:129], v[130:133], v[162:165], v[126:129]
	v_mfma_f32_16x16x32_bf16 v[122:125], v[150:153], v[162:165], v[122:125]
	v_mfma_f32_16x16x32_bf16 v[118:121], v[130:133], v[170:173], v[118:121]
	v_mfma_f32_16x16x32_bf16 v[114:117], v[150:153], v[170:173], v[114:117]
	v_mfma_f32_16x16x32_bf16 v[110:113], v[130:133], v[178:181], v[110:113]
	v_mfma_f32_16x16x32_bf16 v[106:109], v[150:153], v[178:181], v[106:109]
	v_mfma_f32_16x16x32_bf16 v[102:105], v[130:133], v[186:189], v[102:105]
	v_mfma_f32_16x16x32_bf16 v[98:101], v[150:153], v[186:189], v[98:101]
	v_mfma_f32_16x16x32_bf16 v[126:129], v[134:137], v[166:169], v[126:129]
	v_mfma_f32_16x16x32_bf16 v[122:125], v[158:161], v[166:169], v[122:125]
	v_mfma_f32_16x16x32_bf16 v[118:121], v[134:137], v[174:177], v[118:121]
	v_mfma_f32_16x16x32_bf16 v[114:117], v[158:161], v[174:177], v[114:117]
	v_mfma_f32_16x16x32_bf16 v[110:113], v[134:137], v[182:185], v[110:113]
	v_mfma_f32_16x16x32_bf16 v[106:109], v[158:161], v[182:185], v[106:109]
	v_mfma_f32_16x16x32_bf16 v[102:105], v[134:137], v[190:193], v[102:105]
	v_mfma_f32_16x16x32_bf16 v[98:101], v[158:161], v[190:193], v[98:101]
	s_setprio 0
	s_barrier
	s_add_i32 vcc_lo, 0, 0x14040
	s_add_i32 s96, s96, s65
	v_add_u32_e32 v194, vcc_lo, v156
	v_lshl_add_u64 v[214:215], s[56:57], 0, v[140:141]
	s_mov_b32 m0, s96
	ds_read_b128 v[198:201], v194
	ds_read_b128 v[202:205], v194 offset:1024
	ds_read_b128 v[206:209], v194 offset:2048
	ds_read_b128 v[210:213], v194 offset:3072
	global_load_lds_dwordx4 v[214:215], off
	v_lshl_add_u64 v[216:217], s[56:57], 0, v[144:145]
	s_add_i32 m0, s96, 0x2000
	s_nop 0
	global_load_lds_dwordx4 v[216:217], off
	s_barrier
	s_waitcnt lgkmcnt(0)
	s_setprio 1
	s_waitcnt lgkmcnt(0)
	v_mfma_f32_16x16x32_bf16 v[62:65], v[198:201], v[162:165], v[62:65]
	v_mfma_f32_16x16x32_bf16 v[58:61], v[206:209], v[162:165], v[58:61]
	v_mfma_f32_16x16x32_bf16 v[54:57], v[198:201], v[170:173], v[54:57]
	v_mfma_f32_16x16x32_bf16 v[50:53], v[206:209], v[170:173], v[50:53]
	v_mfma_f32_16x16x32_bf16 v[46:49], v[198:201], v[178:181], v[46:49]
	v_mfma_f32_16x16x32_bf16 v[42:45], v[206:209], v[178:181], v[42:45]
	v_mfma_f32_16x16x32_bf16 v[38:41], v[198:201], v[186:189], v[38:41]
	v_mfma_f32_16x16x32_bf16 v[34:37], v[206:209], v[186:189], v[34:37]
	v_mfma_f32_16x16x32_bf16 v[62:65], v[202:205], v[166:169], v[62:65]
	v_mfma_f32_16x16x32_bf16 v[58:61], v[210:213], v[166:169], v[58:61]
	v_mfma_f32_16x16x32_bf16 v[54:57], v[202:205], v[174:177], v[54:57]
	v_mfma_f32_16x16x32_bf16 v[50:53], v[210:213], v[174:177], v[50:53]
	v_mfma_f32_16x16x32_bf16 v[46:49], v[202:205], v[182:185], v[46:49]
	v_mfma_f32_16x16x32_bf16 v[42:45], v[210:213], v[182:185], v[42:45]
	v_mfma_f32_16x16x32_bf16 v[38:41], v[202:205], v[190:193], v[38:41]
	v_mfma_f32_16x16x32_bf16 v[34:37], v[210:213], v[190:193], v[34:37]
	s_setprio 0
	s_mov_b32 m0, s67
	v_lshl_add_u64 v[218:219], s[58:59], 0, v[138:139]
	s_barrier
	ds_read_b128 v[162:165], v157 offset:16448
	ds_read_b128 v[166:169], v157 offset:17472
	ds_read_b128 v[170:173], v157 offset:18496
	ds_read_b128 v[174:177], v157 offset:19520
	ds_read_b128 v[178:181], v157 offset:20544
	ds_read_b128 v[182:185], v157 offset:21568
	ds_read_b128 v[186:189], v157 offset:22592
	ds_read_b128 v[190:193], v157 offset:23616
	global_load_lds_dwordx4 v[218:219], off
	v_lshl_add_u64 v[238:239], s[58:59], 0, v[142:143]
	s_mov_b32 m0, s68
	s_nop 0
	global_load_lds_dwordx4 v[238:239], off
	s_barrier
	s_waitcnt lgkmcnt(0)
	s_setprio 1
	s_waitcnt lgkmcnt(0)
	v_mfma_f32_16x16x32_bf16 v[94:97], v[130:133], v[162:165], v[94:97]
	v_mfma_f32_16x16x32_bf16 v[90:93], v[150:153], v[162:165], v[90:93]
	v_mfma_f32_16x16x32_bf16 v[86:89], v[130:133], v[170:173], v[86:89]
	v_mfma_f32_16x16x32_bf16 v[82:85], v[150:153], v[170:173], v[82:85]
	v_mfma_f32_16x16x32_bf16 v[78:81], v[130:133], v[178:181], v[78:81]
	v_mfma_f32_16x16x32_bf16 v[74:77], v[150:153], v[178:181], v[74:77]
	v_mfma_f32_16x16x32_bf16 v[70:73], v[130:133], v[186:189], v[70:73]
	v_mfma_f32_16x16x32_bf16 v[66:69], v[150:153], v[186:189], v[66:69]
	v_mfma_f32_16x16x32_bf16 v[94:97], v[134:137], v[166:169], v[94:97]
	v_mfma_f32_16x16x32_bf16 v[90:93], v[158:161], v[166:169], v[90:93]
	v_mfma_f32_16x16x32_bf16 v[86:89], v[134:137], v[174:177], v[86:89]
	v_mfma_f32_16x16x32_bf16 v[82:85], v[158:161], v[174:177], v[82:85]
	v_mfma_f32_16x16x32_bf16 v[78:81], v[134:137], v[182:185], v[78:81]
	v_mfma_f32_16x16x32_bf16 v[74:77], v[158:161], v[182:185], v[74:77]
	v_mfma_f32_16x16x32_bf16 v[70:73], v[134:137], v[190:193], v[70:73]
	v_mfma_f32_16x16x32_bf16 v[66:69], v[158:161], v[190:193], v[66:69]
	s_setprio 0
	s_barrier
	s_add_u32 s96, s56, 0x40000
	s_addc_u32 s97, s57, 0
	s_add_i32 vcc_lo, vcc_lo, s65
	v_lshl_add_u64 v[130:131], s[96:97], 0, v[140:141]
	s_mov_b32 m0, vcc_lo
	s_nop 0
	global_load_lds_dwordx4 v[130:131], off
	v_lshl_add_u64 v[130:131], s[96:97], 0, v[144:145]
	s_add_i32 m0, vcc_lo, 0x2000
	s_nop 0
	global_load_lds_dwordx4 v[130:131], off
	s_waitcnt vmcnt(6)
	s_barrier
	s_setprio 1
	v_mfma_f32_16x16x32_bf16 v[30:33], v[198:201], v[162:165], v[30:33]
	v_mfma_f32_16x16x32_bf16 v[26:29], v[206:209], v[162:165], v[26:29]
	v_mfma_f32_16x16x32_bf16 v[22:25], v[198:201], v[170:173], v[22:25]
	v_mfma_f32_16x16x32_bf16 v[18:21], v[206:209], v[170:173], v[18:21]
	v_mfma_f32_16x16x32_bf16 v[14:17], v[198:201], v[178:181], v[14:17]
	v_mfma_f32_16x16x32_bf16 v[10:13], v[206:209], v[178:181], v[10:13]
	v_mfma_f32_16x16x32_bf16 v[6:9], v[198:201], v[186:189], v[6:9]
	v_mfma_f32_16x16x32_bf16 v[2:5], v[206:209], v[186:189], v[2:5]
	v_mfma_f32_16x16x32_bf16 v[30:33], v[202:205], v[166:169], v[30:33]
	v_mfma_f32_16x16x32_bf16 v[26:29], v[210:213], v[166:169], v[26:29]
	v_mfma_f32_16x16x32_bf16 v[22:25], v[202:205], v[174:177], v[22:25]
	v_mfma_f32_16x16x32_bf16 v[18:21], v[210:213], v[174:177], v[18:21]
	v_mfma_f32_16x16x32_bf16 v[14:17], v[202:205], v[182:185], v[14:17]
	v_mfma_f32_16x16x32_bf16 v[10:13], v[210:213], v[182:185], v[10:13]
	v_mfma_f32_16x16x32_bf16 v[6:9], v[202:205], v[190:193], v[6:9]
	v_mfma_f32_16x16x32_bf16 v[2:5], v[210:213], v[190:193], v[2:5]
	s_setprio 0
	s_add_i32 s96, 0, 0x18040
	v_add_u32_e32 v158, s96, v156
	s_barrier
	ds_read_b128 v[130:133], v158
	ds_read_b128 v[134:137], v158 offset:1024
	ds_read_b128 v[150:153], v158 offset:2048
	ds_read_b128 v[158:161], v158 offset:3072
	s_add_u32 s58, s58, 0x40000
	s_addc_u32 s59, s59, 0
	s_mov_b32 m0, s69
	v_lshl_add_u64 v[198:199], s[58:59], 0, v[138:139]
	ds_read_b128 v[162:165], v157 offset:32832
	ds_read_b128 v[166:169], v157 offset:33856
	ds_read_b128 v[170:173], v157 offset:34880
	ds_read_b128 v[174:177], v157 offset:35904
	ds_read_b128 v[178:181], v157 offset:36928
	ds_read_b128 v[182:185], v157 offset:37952
	ds_read_b128 v[186:189], v157 offset:38976
	ds_read_b128 v[190:193], v157 offset:40000
	global_load_lds_dwordx4 v[198:199], off
	v_lshl_add_u64 v[198:199], s[58:59], 0, v[142:143]
	s_mov_b32 m0, s70
	s_nop 0
	global_load_lds_dwordx4 v[198:199], off
	s_waitcnt lgkmcnt(8)
	s_barrier
	s_waitcnt lgkmcnt(0)
	s_setprio 1
	s_waitcnt lgkmcnt(0)
	v_mfma_f32_16x16x32_bf16 v[126:129], v[130:133], v[162:165], v[126:129]
	v_mfma_f32_16x16x32_bf16 v[122:125], v[150:153], v[162:165], v[122:125]
	v_mfma_f32_16x16x32_bf16 v[118:121], v[130:133], v[170:173], v[118:121]
	v_mfma_f32_16x16x32_bf16 v[114:117], v[150:153], v[170:173], v[114:117]
	v_mfma_f32_16x16x32_bf16 v[110:113], v[130:133], v[178:181], v[110:113]
	v_mfma_f32_16x16x32_bf16 v[106:109], v[150:153], v[178:181], v[106:109]
	v_mfma_f32_16x16x32_bf16 v[102:105], v[130:133], v[186:189], v[102:105]
	v_mfma_f32_16x16x32_bf16 v[98:101], v[150:153], v[186:189], v[98:101]
	v_mfma_f32_16x16x32_bf16 v[126:129], v[134:137], v[166:169], v[126:129]
	v_mfma_f32_16x16x32_bf16 v[122:125], v[158:161], v[166:169], v[122:125]
	v_mfma_f32_16x16x32_bf16 v[118:121], v[134:137], v[174:177], v[118:121]
	v_mfma_f32_16x16x32_bf16 v[114:117], v[158:161], v[174:177], v[114:117]
	v_mfma_f32_16x16x32_bf16 v[110:113], v[134:137], v[182:185], v[110:113]
	v_mfma_f32_16x16x32_bf16 v[106:109], v[158:161], v[182:185], v[106:109]
	v_mfma_f32_16x16x32_bf16 v[102:105], v[134:137], v[190:193], v[102:105]
	v_mfma_f32_16x16x32_bf16 v[98:101], v[158:161], v[190:193], v[98:101]
	s_setprio 0
	s_barrier
	s_add_i32 s58, 0, 0x1c040
	s_add_i32 s59, s96, s65
	v_add_u32_e32 v194, s58, v156
	v_lshl_add_u64 v[214:215], v[214:215], 0, s[10:11]
	s_mov_b32 m0, s59
	ds_read_b128 v[198:201], v194
	ds_read_b128 v[202:205], v194 offset:1024
	ds_read_b128 v[206:209], v194 offset:2048
	ds_read_b128 v[210:213], v194 offset:3072
	global_load_lds_dwordx4 v[214:215], off
	v_lshl_add_u64 v[214:215], v[216:217], 0, s[10:11]
	s_add_i32 m0, s59, 0x2000
	s_nop 0
	global_load_lds_dwordx4 v[214:215], off
	s_barrier
	s_waitcnt lgkmcnt(0)
	s_setprio 1
	s_waitcnt lgkmcnt(0)
	v_mfma_f32_16x16x32_bf16 v[62:65], v[198:201], v[162:165], v[62:65]
	v_mfma_f32_16x16x32_bf16 v[58:61], v[206:209], v[162:165], v[58:61]
	v_mfma_f32_16x16x32_bf16 v[54:57], v[198:201], v[170:173], v[54:57]
	v_mfma_f32_16x16x32_bf16 v[50:53], v[206:209], v[170:173], v[50:53]
	v_mfma_f32_16x16x32_bf16 v[46:49], v[198:201], v[178:181], v[46:49]
	v_mfma_f32_16x16x32_bf16 v[42:45], v[206:209], v[178:181], v[42:45]
	v_mfma_f32_16x16x32_bf16 v[38:41], v[198:201], v[186:189], v[38:41]
	v_mfma_f32_16x16x32_bf16 v[34:37], v[206:209], v[186:189], v[34:37]
	v_mfma_f32_16x16x32_bf16 v[62:65], v[202:205], v[166:169], v[62:65]
	v_mfma_f32_16x16x32_bf16 v[58:61], v[210:213], v[166:169], v[58:61]
	v_mfma_f32_16x16x32_bf16 v[54:57], v[202:205], v[174:177], v[54:57]
	v_mfma_f32_16x16x32_bf16 v[50:53], v[210:213], v[174:177], v[50:53]
	v_mfma_f32_16x16x32_bf16 v[46:49], v[202:205], v[182:185], v[46:49]
	v_mfma_f32_16x16x32_bf16 v[42:45], v[210:213], v[182:185], v[42:45]
	v_mfma_f32_16x16x32_bf16 v[38:41], v[202:205], v[190:193], v[38:41]
	v_mfma_f32_16x16x32_bf16 v[34:37], v[210:213], v[190:193], v[34:37]
	s_setprio 0
	s_mov_b32 m0, s83
	v_lshl_add_u64 v[214:215], v[218:219], 0, s[10:11]
	s_barrier
	ds_read_b128 v[162:165], v157 offset:49216
	ds_read_b128 v[166:169], v157 offset:50240
	ds_read_b128 v[170:173], v157 offset:51264
	ds_read_b128 v[174:177], v157 offset:52288
	ds_read_b128 v[178:181], v157 offset:53312
	ds_read_b128 v[182:185], v157 offset:54336
	ds_read_b128 v[186:189], v157 offset:55360
	ds_read_b128 v[190:193], v157 offset:56384
	global_load_lds_dwordx4 v[214:215], off
	v_lshl_add_u64 v[214:215], v[238:239], 0, s[10:11]
	s_mov_b32 m0, s84
	s_nop 0
	global_load_lds_dwordx4 v[214:215], off
	s_barrier
	s_waitcnt lgkmcnt(0)
	s_setprio 1
	s_waitcnt lgkmcnt(0)
	v_mfma_f32_16x16x32_bf16 v[94:97], v[130:133], v[162:165], v[94:97]
	v_mfma_f32_16x16x32_bf16 v[90:93], v[150:153], v[162:165], v[90:93]
	v_mfma_f32_16x16x32_bf16 v[86:89], v[130:133], v[170:173], v[86:89]
	v_mfma_f32_16x16x32_bf16 v[82:85], v[150:153], v[170:173], v[82:85]
	v_mfma_f32_16x16x32_bf16 v[78:81], v[130:133], v[178:181], v[78:81]
	v_mfma_f32_16x16x32_bf16 v[74:77], v[150:153], v[178:181], v[74:77]
	v_mfma_f32_16x16x32_bf16 v[70:73], v[130:133], v[186:189], v[70:73]
	v_mfma_f32_16x16x32_bf16 v[66:69], v[150:153], v[186:189], v[66:69]
	v_mfma_f32_16x16x32_bf16 v[94:97], v[134:137], v[166:169], v[94:97]
	v_mfma_f32_16x16x32_bf16 v[90:93], v[158:161], v[166:169], v[90:93]
	v_mfma_f32_16x16x32_bf16 v[86:89], v[134:137], v[174:177], v[86:89]
	v_mfma_f32_16x16x32_bf16 v[82:85], v[158:161], v[174:177], v[82:85]
	v_mfma_f32_16x16x32_bf16 v[78:81], v[134:137], v[182:185], v[78:81]
	v_mfma_f32_16x16x32_bf16 v[74:77], v[158:161], v[182:185], v[74:77]
	v_mfma_f32_16x16x32_bf16 v[70:73], v[134:137], v[190:193], v[70:73]
	v_mfma_f32_16x16x32_bf16 v[66:69], v[158:161], v[190:193], v[66:69]
	s_setprio 0
	s_barrier
	s_add_u32 s56, s56, 0x40080
	s_addc_u32 s57, s57, 0
	s_add_i32 s58, s58, s65
	v_lshl_add_u64 v[130:131], s[56:57], 0, v[140:141]
	s_mov_b32 m0, s58
	s_nop 0
	global_load_lds_dwordx4 v[130:131], off
	v_lshl_add_u64 v[130:131], s[56:57], 0, v[144:145]
	s_add_i32 m0, s58, 0x2000
	s_nop 0
	global_load_lds_dwordx4 v[130:131], off
	s_waitcnt vmcnt(6)
	s_barrier
	s_setprio 1
	v_mfma_f32_16x16x32_bf16 v[30:33], v[198:201], v[162:165], v[30:33]
	v_mfma_f32_16x16x32_bf16 v[26:29], v[206:209], v[162:165], v[26:29]
	v_mfma_f32_16x16x32_bf16 v[22:25], v[198:201], v[170:173], v[22:25]
	v_mfma_f32_16x16x32_bf16 v[18:21], v[206:209], v[170:173], v[18:21]
	v_mfma_f32_16x16x32_bf16 v[14:17], v[198:201], v[178:181], v[14:17]
	v_mfma_f32_16x16x32_bf16 v[10:13], v[206:209], v[178:181], v[10:13]
	v_mfma_f32_16x16x32_bf16 v[6:9], v[198:201], v[186:189], v[6:9]
	v_mfma_f32_16x16x32_bf16 v[2:5], v[206:209], v[186:189], v[2:5]
	v_mfma_f32_16x16x32_bf16 v[30:33], v[202:205], v[166:169], v[30:33]
	v_mfma_f32_16x16x32_bf16 v[26:29], v[210:213], v[166:169], v[26:29]
	v_mfma_f32_16x16x32_bf16 v[22:25], v[202:205], v[174:177], v[22:25]
	v_mfma_f32_16x16x32_bf16 v[18:21], v[210:213], v[174:177], v[18:21]
	v_mfma_f32_16x16x32_bf16 v[14:17], v[202:205], v[182:185], v[14:17]
	v_mfma_f32_16x16x32_bf16 v[10:13], v[210:213], v[182:185], v[10:13]
	v_mfma_f32_16x16x32_bf16 v[6:9], v[202:205], v[190:193], v[6:9]
	v_mfma_f32_16x16x32_bf16 v[2:5], v[210:213], v[190:193], v[2:5]
	s_setprio 0
	s_add_i32 s51, s51, 2
	s_add_u32 s37, s37, 0x100
	s_addc_u32 s49, s49, 0
	s_add_u32 s38, s38, 0x100
	s_addc_u32 s39, s39, 0
	s_cmp_gt_u32 s51, 13
	s_barrier
	s_cbranch_scc0 .LBB0_344
	s_lshl_b32 s9, s34, 8
	s_or_b32 s9, s9, s82
	v_or_b32_e32 v152, s9, v155
	s_movk_i32 s14, 0x1cc0
	v_lshl_add_u32 v150, s36, 8, v154
	v_cmp_gt_i32_e32 vcc, s14, v152
	v_ashrrev_i32_e32 v153, 31, v152
	s_and_saveexec_b64 s[34:35], vcc
	s_movk_i32 s97, 0x3000
	s_cbranch_execz .LBB0_362
	v_mov_b32_e32 v134, v240
	v_mov_b32_e32 v135, v241
	v_mov_b32_e32 v136, v242
	v_mov_b32_e32 v137, v243
	v_mov_b32_e32 v130, v244
	v_mov_b32_e32 v131, v245
	v_mov_b32_e32 v132, v246
	v_mov_b32_e32 v133, v247
	v_mov_b64_e32 v[158:159], s[46:47]
	s_cmpk_eq_i32 s9, 0x800
	v_mad_i64_i32 v[162:163], s[14:15], v150, s2, v[158:159]
	v_mov_b32_e32 v194, v152
	s_cselect_b64 s[38:39], -1, 0
	s_cmpk_lg_i32 s9, 0x800
	v_lshl_add_u64 v[162:163], v[152:153], 1, v[162:163]
	s_nop 0
	v_pk_add_f32 v[128:129], v[128:129], v[136:137]
	v_pk_add_f32 v[126:127], v[126:127], v[134:135]
	v_pk_add_f32 v[124:125], v[124:125], v[132:133]
	v_pk_add_f32 v[122:123], v[122:123], v[130:131]
	v_cvt_pk_bf16_f32 v158, v126, v127
	v_cvt_pk_bf16_f32 v159, v128, v129
	v_cvt_pk_bf16_f32 v161, v124, v125
	s_nop 0
	v_cvt_pk_bf16_f32 v160, v122, v123
	global_store_dwordx4 v[162:163], v[158:161], off
	s_cbranch_scc1 .LBB0_348
	v_ashrrev_i32_e32 v151, 31, v150
	v_lshlrev_b64 v[158:159], 7, v[150:151]
	v_lshl_add_u64 v[158:159], s[40:41], 0, v[158:159]
	v_lshl_add_u64 v[158:159], v[194:195], 2, v[158:159]
	v_add_co_u32_e32 v160, vcc, 0xffffe000, v158
	s_nop 1
	v_addc_co_u32_e32 v161, vcc, -1, v159, vcc
	global_store_dwordx4 v[160:161], v[126:129], off
	s_nop 1
	v_add_co_u32_e32 v126, vcc, 0xfffff000, v158
	s_nop 1
	v_addc_co_u32_e32 v127, vcc, -1, v159, vcc
	global_store_dwordx4 v[126:127], v[122:125], off offset:-4080

.LBB0_362:
	s_or_b64 exec, exec, s[34:35]
	s_nop 0
	v_or_b32_e32 v66, 0x80, v152
	s_movk_i32 s9, 0x1cc0
	v_cmp_gt_i32_e32 vcc, s9, v66
	s_and_saveexec_b64 s[34:35], vcc
	s_cbranch_execz .LBB0_336
	v_mov_b32_e32 v66, v222
	v_mov_b32_e32 v67, v223
	v_mov_b32_e32 v68, v224
	v_mov_b32_e32 v69, v225
	v_mov_b32_e32 v70, v248
	v_mov_b32_e32 v71, v249
	v_mov_b32_e32 v72, v250
	v_mov_b32_e32 v73, v251
	v_pk_add_f32 v[58:59], v[58:59], v[66:67]
	v_pk_add_f32 v[64:65], v[64:65], v[72:73]
	v_pk_add_f32 v[62:63], v[62:63], v[70:71]
	v_pk_add_f32 v[60:61], v[60:61], v[68:69]
	v_cvt_pk_bf16_f32 v62, v62, v63
	v_cvt_pk_bf16_f32 v63, v64, v65
	v_cvt_pk_bf16_f32 v64, v58, v59
	v_mov_b64_e32 v[58:59], s[46:47]
	v_cvt_pk_bf16_f32 v65, v60, v61
	v_mad_i64_i32 v[74:75], s[14:15], v150, s2, v[58:59]
	v_lshlrev_b64 v[60:61], 1, v[152:153]
	v_lshl_add_u64 v[74:75], v[74:75], 0, v[60:61]
	global_store_dwordx4 v[74:75], v[62:65], off offset:256
	v_pk_add_f32 v[54:55], v[54:55], v[70:71]
	v_pk_add_f32 v[56:57], v[56:57], v[72:73]
	v_or_b32_e32 v64, 16, v150
	v_pk_add_f32 v[62:63], v[52:53], v[68:69]
	v_pk_add_f32 v[52:53], v[50:51], v[66:67]
	v_cvt_pk_bf16_f32 v50, v54, v55
	v_mad_i64_i32 v[54:55], s[14:15], v64, s2, v[58:59]
	v_cvt_pk_bf16_f32 v52, v52, v53
	v_lshl_add_u64 v[54:55], v[54:55], 0, v[60:61]
	v_cvt_pk_bf16_f32 v51, v56, v57
	v_cvt_pk_bf16_f32 v53, v62, v63
	global_store_dwordx4 v[54:55], v[50:53], off offset:256
	v_pk_add_f32 v[46:47], v[46:47], v[70:71]
	v_pk_add_f32 v[48:49], v[48:49], v[72:73]
	v_or_b32_e32 v52, 32, v150
	v_pk_add_f32 v[50:51], v[44:45], v[68:69]
	v_pk_add_f32 v[44:45], v[42:43], v[66:67]
	v_cvt_pk_bf16_f32 v42, v46, v47
	v_mad_i64_i32 v[46:47], s[14:15], v52, s2, v[58:59]
	v_cvt_pk_bf16_f32 v44, v44, v45
	v_lshl_add_u64 v[46:47], v[46:47], 0, v[60:61]
	v_cvt_pk_bf16_f32 v43, v48, v49
	v_cvt_pk_bf16_f32 v45, v50, v51
	global_store_dwordx4 v[46:47], v[42:45], off offset:256
	v_pk_add_f32 v[38:39], v[38:39], v[70:71]
	v_pk_add_f32 v[40:41], v[40:41], v[72:73]
	v_or_b32_e32 v44, 48, v150
	v_pk_add_f32 v[42:43], v[36:37], v[68:69]
	v_pk_add_f32 v[36:37], v[34:35], v[66:67]
	v_cvt_pk_bf16_f32 v34, v38, v39
	v_mad_i64_i32 v[38:39], s[14:15], v44, s2, v[58:59]
	v_cvt_pk_bf16_f32 v36, v36, v37
	v_lshl_add_u64 v[38:39], v[38:39], 0, v[60:61]
	v_cvt_pk_bf16_f32 v35, v40, v41
	v_cvt_pk_bf16_f32 v37, v42, v43
	global_store_dwordx4 v[38:39], v[34:37], off offset:256
	v_pk_add_f32 v[30:31], v[30:31], v[70:71]
	v_pk_add_f32 v[32:33], v[32:33], v[72:73]
	v_add_u32_e32 v36, 0x80, v150
	v_pk_add_f32 v[34:35], v[28:29], v[68:69]
	v_pk_add_f32 v[28:29], v[26:27], v[66:67]
	v_cvt_pk_bf16_f32 v26, v30, v31
	v_mad_i64_i32 v[30:31], s[14:15], v36, s2, v[58:59]
	v_cvt_pk_bf16_f32 v28, v28, v29
	v_lshl_add_u64 v[30:31], v[30:31], 0, v[60:61]
	v_cvt_pk_bf16_f32 v27, v32, v33
	v_cvt_pk_bf16_f32 v29, v34, v35
	global_store_dwordx4 v[30:31], v[26:29], off offset:256
	v_pk_add_f32 v[22:23], v[22:23], v[70:71]
	v_pk_add_f32 v[24:25], v[24:25], v[72:73]
	v_add_u32_e32 v28, 0x90, v150
	v_pk_add_f32 v[26:27], v[20:21], v[68:69]
	v_pk_add_f32 v[20:21], v[18:19], v[66:67]
	v_cvt_pk_bf16_f32 v18, v22, v23
	v_mad_i64_i32 v[22:23], s[14:15], v28, s2, v[58:59]
	v_cvt_pk_bf16_f32 v20, v20, v21
	v_lshl_add_u64 v[22:23], v[22:23], 0, v[60:61]
	v_cvt_pk_bf16_f32 v19, v24, v25
	v_cvt_pk_bf16_f32 v21, v26, v27
	global_store_dwordx4 v[22:23], v[18:21], off offset:256
	v_pk_add_f32 v[14:15], v[14:15], v[70:71]
	v_pk_add_f32 v[16:17], v[16:17], v[72:73]
	v_add_u32_e32 v20, 0xa0, v150
	v_pk_add_f32 v[18:19], v[12:13], v[68:69]
	v_pk_add_f32 v[12:13], v[10:11], v[66:67]
	v_cvt_pk_bf16_f32 v10, v14, v15
	v_mad_i64_i32 v[14:15], s[14:15], v20, s2, v[58:59]
	v_cvt_pk_bf16_f32 v12, v12, v13
	v_lshl_add_u64 v[14:15], v[14:15], 0, v[60:61]
	v_cvt_pk_bf16_f32 v11, v16, v17
	v_cvt_pk_bf16_f32 v13, v18, v19
	global_store_dwordx4 v[14:15], v[10:13], off offset:256
	v_pk_add_f32 v[6:7], v[6:7], v[70:71]
	v_pk_add_f32 v[8:9], v[8:9], v[72:73]
	v_add_u32_e32 v12, 0xb0, v150
	v_pk_add_f32 v[10:11], v[4:5], v[68:69]
	v_pk_add_f32 v[4:5], v[2:3], v[66:67]
	v_cvt_pk_bf16_f32 v2, v6, v7
	v_mad_i64_i32 v[6:7], s[14:15], v12, s2, v[58:59]
	v_lshl_add_u64 v[6:7], v[6:7], 0, v[60:61]
	v_cvt_pk_bf16_f32 v3, v8, v9
	v_cvt_pk_bf16_f32 v4, v4, v5
	v_cvt_pk_bf16_f32 v5, v10, v11
	global_store_dwordx4 v[6:7], v[2:5], off offset:256
	s_branch .LBB0_336
